# last 4096 PEER table rows converted by workgroups 64..255 in P3 (idle while 0..63 run the compress GEMM) instead of in the HBM-bound P10
# baseline (speedup 1.0000x reference)
; __device__ __forceinline__ void phase_peer_tables(const Frame& F, const Args& a, int r_lo, int r_hi, int gw, int NGW) {
;     unsigned char* PT = a.ws + WS_PT; const int lane = F.lane;
;     int r = r_lo + gw; if (r >= r_hi) return;
;     f32x4 vA[16], vB[16];
;     pt_load(a.in[17], a.in[18], vA, r, lane);
;     for (;;) {
;         const int r1 = r + NGW; const bool h1 = r1 < r_hi;
;         if (h1) pt_load(a.in[17], a.in[18], vB, r1, lane);
.Lpt3_entry:
	s_load_dwordx4 s[12:15], s[86:87], 0x88
	s_load_dwordx2 s[2:3], s[86:87], 0xc0
	s_sub_i32 s45, s94, 64
	s_movk_i32 s44, 0xc0
	s_lshl_b32 s0, s45, 3
	v_readlane_b32 s1, v245, 7
	s_add_i32 s4, s1, s0
	s_movk_i32 s0, 0x600
	v_cmp_eq_u32_e64 s[6:7], 0, v194
	s_waitcnt vmcnt(0) lgkmcnt(0)
	s_movk_i32 s5, 0x7000
	s_add_i32 s41, s5, s4
	s_cmpk_gt_i32 s41, 0x7fff
	s_movk_i32 s4, 0x3000
	s_cbranch_scc1 .Lpt3_end
	s_add_u32 s1, s2, 0x3ba00000
	s_addc_u32 s10, s3, 0
	s_cmpk_lt_u32 s41, 0x4000
	s_cselect_b32 s3, s13, s15
	s_cselect_b32 s2, s12, s14
	s_lshl_b32 s8, s41, 14
	s_and_b32 s8, s8, 0xfffc000
	s_add_u32 s2, s2, s8
	v_mov_b32_e32 v133, 0
	s_addc_u32 s3, s3, 0
	v_lshlrev_b32_e32 v130, 4, v194
	v_mov_b32_e32 v131, v133
	v_lshl_add_u64 v[26:27], s[2:3], 0, v[130:131]
	s_movk_i32 s11, 0x1000
	v_add_co_u32_e32 v66, vcc, s11, v26
	s_movk_i32 s8, 0x2000
	s_nop 0
	v_addc_co_u32_e32 v67, vcc, 0, v27, vcc
	v_add_co_u32_e32 v28, vcc, s8, v26
	global_load_dwordx4 v[2:5], v130, s[2:3] offset:1024
	global_load_dwordx4 v[6:9], v130, s[2:3] offset:2048
	v_addc_co_u32_e32 v29, vcc, 0, v27, vcc
	global_load_dwordx4 v[10:13], v130, s[2:3] offset:3072
	global_load_dwordx4 v[14:17], v[28:29], off offset:-4096
	global_load_dwordx4 v[18:21], v[66:67], off offset:1024
	global_load_dwordx4 v[22:25], v[66:67], off offset:2048
	global_load_dwordx4 v[30:33], v[28:29], off
	global_load_dwordx4 v[38:41], v[28:29], off offset:1024
	global_load_dwordx4 v[42:45], v[28:29], off offset:2048
	global_load_dwordx4 v[46:49], v[28:29], off offset:3072
	v_add_co_u32_e32 v68, vcc, s4, v26
	v_mbcnt_lo_u32_b32 v1, -1, 0
	s_nop 0
	v_addc_co_u32_e32 v69, vcc, 0, v27, vcc
	global_load_dwordx4 v[34:37], v[66:67], off offset:3072
	global_load_dwordx4 v[50:53], v[68:69], off
	global_load_dwordx4 v[54:57], v[68:69], off offset:1024
	global_load_dwordx4 v[58:61], v[68:69], off offset:2048
	global_load_dwordx4 v[26:29], v130, s[2:3]
	global_load_dwordx4 v[62:65], v[68:69], off offset:3072
	v_mbcnt_hi_u32_b32 v66, -1, v1
	v_and_b32_e32 v1, 64, v66
	v_add_u32_e32 v67, 64, v1
	v_xor_b32_e32 v1, 1, v66
	v_cmp_lt_i32_e32 vcc, v1, v67
	v_xor_b32_e32 v68, 2, v66
	s_lshl_b32 s2, s45, 15
	v_cndmask_b32_e32 v1, v66, v1, vcc
	v_cmp_lt_i32_e32 vcc, v68, v67
	s_lshl_b32 s3, s5, 12
	s_add_i32 s2, s2, s3
	v_cndmask_b32_e32 v68, v66, v68, vcc
	v_lshlrev_b32_e32 v136, 2, v68
	v_xor_b32_e32 v68, 4, v66
	v_cmp_lt_i32_e32 vcc, v68, v67
	v_readlane_b32 s3, v245, 7
	s_lshl_b32 s3, s3, 12
	v_cndmask_b32_e32 v68, v66, v68, vcc
	v_lshlrev_b32_e32 v137, 2, v68
	v_xor_b32_e32 v68, 8, v66
	v_cmp_lt_i32_e32 vcc, v68, v67
	v_lshlrev_b32_e32 v1, 2, v1
	s_lshl_b32 s16, s44, 4
	v_cndmask_b32_e32 v68, v66, v68, vcc
	v_lshlrev_b32_e32 v138, 2, v68
	v_xor_b32_e32 v68, 16, v66
	v_cmp_lt_i32_e32 vcc, v68, v67
	s_lshl_b32 s17, s44, 16
	s_add_i32 s20, s2, s3
	v_cndmask_b32_e32 v68, v66, v68, vcc
	v_lshlrev_b32_e32 v139, 2, v68
	v_xor_b32_e32 v68, 32, v66
	v_cmp_lt_i32_e32 vcc, v68, v67
	s_lshl_b32 s21, s44, 15
	s_mov_b32 s22, 0x42fe0000
	v_cndmask_b32_e32 v66, v66, v68, vcc
	v_lshlrev_b32_e32 v140, 2, v66
	s_mov_b32 s23, 0x40c0c00
	s_mov_b32 s24, 0x400000
	s_mov_b32 s25, 0x800000
	s_mov_b32 s26, 0xc00000
	s_mov_b32 s27, 0x1000000
	s_mov_b32 s28, 0x1400000
	s_mov_b32 s29, 0x1800000
	s_mov_b32 s30, 0x1c00000
	s_brev_b32 s31, 64
	s_mov_b32 s33, 0x2400000
	s_mov_b32 s34, 0x2800000
	s_mov_b32 s35, 0x2c00000
	s_mov_b32 s36, 0x3000000
	s_mov_b32 s37, 0x3400000
	s_mov_b32 s38, 0x3800000
	s_brev_b32 s39, 16
	s_branch .Lpt3_1252

; __device__ __forceinline__ void phase_peer_tables(const Frame& F, const Args& a, int r_lo, int r_hi, int gw, int NGW) {
;     unsigned char* PT = a.ws + WS_PT; const int lane = F.lane;
;     int r = r_lo + gw; if (r >= r_hi) return;
;     f32x4 vA[16], vB[16];
;     pt_load(a.in[17], a.in[18], vA, r, lane);
;     for (;;) {
;         const int r1 = r + NGW; const bool h1 = r1 < r_hi;
;         if (h1) pt_load(a.in[17], a.in[18], vB, r1, lane);
;         pt_proc(PT, vA, r, lane);
;         if (!h1) break;
;         const int r2 = r1 + NGW; const bool h2 = r2 < r_hi;
;         if (h2) pt_load(a.in[17], a.in[18], vA, r2, lane);
;         pt_proc(PT, vB, r1, lane);
;         if (!h2) break;
;         r = r2;
;     }
; }
.Lpt3_end:
	s_branch .LBB0_331

; __device__ __forceinline__ void phase_peer_tables(const Frame& F, const Args& a, int r_lo, int r_hi, int gw, int NGW) {
;     unsigned char* PT = a.ws + WS_PT; const int lane = F.lane;
;     int r = r_lo + gw; if (r >= r_hi) return;
;     f32x4 vA[16], vB[16];
;     pt_load(a.in[17], a.in[18], vA, r, lane);
; __global__ void __launch_bounds__(NTHREADS, 2) fwd(Args args) {
;     ...
;         phase_peer_tables(F, args, ((F.G == 256) ? PT_SIDE_ROWS : 0) + PT_EARLY_ROWS, 32768, F.bid * NWAVES + F.wave, F.G * NWAVES);
.LBB0_1248:
	s_cmpk_eq_i32 s96, 0x100
	s_mov_b32 s1, 0x8000
	s_cselect_b32 s5, s1, 0x3000
	s_add_i32 s41, s5, s4
	s_cmpk_gt_i32 s41, 0x7fff
	s_movk_i32 s4, 0x3000
	s_cbranch_scc1 .LBB0_1261
	s_add_u32 s1, s2, 0x3ba00000
	s_addc_u32 s10, s3, 0
	s_cmpk_lt_u32 s41, 0x4000
	s_cselect_b32 s3, s13, s15
	s_cselect_b32 s2, s12, s14
	s_lshl_b32 s8, s41, 14
	s_and_b32 s8, s8, 0xfffc000
	s_add_u32 s2, s2, s8
	v_mov_b32_e32 v133, 0
	s_addc_u32 s3, s3, 0
	v_lshlrev_b32_e32 v130, 4, v194
	v_mov_b32_e32 v131, v133
	v_lshl_add_u64 v[26:27], s[2:3], 0, v[130:131]
	s_movk_i32 s11, 0x1000
	v_add_co_u32_e32 v66, vcc, s11, v26
	s_movk_i32 s8, 0x2000
	s_nop 0
	v_addc_co_u32_e32 v67, vcc, 0, v27, vcc
	v_add_co_u32_e32 v28, vcc, s8, v26
	global_load_dwordx4 v[2:5], v130, s[2:3] offset:1024
	global_load_dwordx4 v[6:9], v130, s[2:3] offset:2048
	v_addc_co_u32_e32 v29, vcc, 0, v27, vcc
	global_load_dwordx4 v[10:13], v130, s[2:3] offset:3072
	global_load_dwordx4 v[14:17], v[28:29], off offset:-4096
	global_load_dwordx4 v[18:21], v[66:67], off offset:1024
	global_load_dwordx4 v[22:25], v[66:67], off offset:2048
	global_load_dwordx4 v[30:33], v[28:29], off
	global_load_dwordx4 v[38:41], v[28:29], off offset:1024
	global_load_dwordx4 v[42:45], v[28:29], off offset:2048
	global_load_dwordx4 v[46:49], v[28:29], off offset:3072
	v_add_co_u32_e32 v68, vcc, s4, v26
	v_mbcnt_lo_u32_b32 v1, -1, 0
	s_nop 0
	v_addc_co_u32_e32 v69, vcc, 0, v27, vcc
	global_load_dwordx4 v[34:37], v[66:67], off offset:3072
	global_load_dwordx4 v[50:53], v[68:69], off
	global_load_dwordx4 v[54:57], v[68:69], off offset:1024
	global_load_dwordx4 v[58:61], v[68:69], off offset:2048
	global_load_dwordx4 v[26:29], v130, s[2:3]
	global_load_dwordx4 v[62:65], v[68:69], off offset:3072
	v_mbcnt_hi_u32_b32 v66, -1, v1
	v_and_b32_e32 v1, 64, v66
	v_add_u32_e32 v67, 64, v1
	v_xor_b32_e32 v1, 1, v66
	v_cmp_lt_i32_e32 vcc, v1, v67
	v_xor_b32_e32 v68, 2, v66
	s_lshl_b32 s2, s94, 15
	v_cndmask_b32_e32 v1, v66, v1, vcc
	v_cmp_lt_i32_e32 vcc, v68, v67
	s_lshl_b32 s3, s5, 12
	s_add_i32 s2, s2, s3
	v_cndmask_b32_e32 v68, v66, v68, vcc
	v_lshlrev_b32_e32 v136, 2, v68
	v_xor_b32_e32 v68, 4, v66
	v_cmp_lt_i32_e32 vcc, v68, v67
	v_readlane_b32 s3, v245, 7
	s_lshl_b32 s3, s3, 12
	v_cndmask_b32_e32 v68, v66, v68, vcc
	v_lshlrev_b32_e32 v137, 2, v68
	v_xor_b32_e32 v68, 8, v66
	v_cmp_lt_i32_e32 vcc, v68, v67
	v_lshlrev_b32_e32 v1, 2, v1
	s_lshl_b32 s16, s96, 4
	v_cndmask_b32_e32 v68, v66, v68, vcc
	v_lshlrev_b32_e32 v138, 2, v68
	v_xor_b32_e32 v68, 16, v66
	v_cmp_lt_i32_e32 vcc, v68, v67
	s_lshl_b32 s17, s96, 16
	s_add_i32 s20, s2, s3
	v_cndmask_b32_e32 v68, v66, v68, vcc
	v_lshlrev_b32_e32 v139, 2, v68
	v_xor_b32_e32 v68, 32, v66
	v_cmp_lt_i32_e32 vcc, v68, v67
	s_lshl_b32 s21, s96, 15
	s_mov_b32 s22, 0x42fe0000
	v_cndmask_b32_e32 v66, v66, v68, vcc
	v_lshlrev_b32_e32 v140, 2, v66
	s_mov_b32 s23, 0x40c0c00
	s_mov_b32 s24, 0x400000
	s_mov_b32 s25, 0x800000
	s_mov_b32 s26, 0xc00000
	s_mov_b32 s27, 0x1000000
	s_mov_b32 s28, 0x1400000
	s_mov_b32 s29, 0x1800000
	s_mov_b32 s30, 0x1c00000
	s_brev_b32 s31, 64
	s_mov_b32 s33, 0x2400000
	s_mov_b32 s34, 0x2800000
	s_mov_b32 s35, 0x2c00000
	s_mov_b32 s36, 0x3000000
	s_mov_b32 s37, 0x3400000
	s_mov_b32 s38, 0x3800000
	s_brev_b32 s39, 16
	s_branch .LBB0_1252
